# in-projection rope epilogue: six of the eight second-half cos/sin loads issued with the first half's loads into spare registers (uses renamed)
# speedup vs baseline: 1.0022x; 1.0011x over previous
.LBB0_684:
	v_lshlrev_b32_e32 v0, 1, v198
	v_and_b32_e32 v0, 0x70, v0
	v_lshl_add_u64 v[202:203], s[46:47], 0, v[0:1]
	v_lshl_add_u64 v[200:201], s[48:49], 0, v[0:1]
	v_lshlrev_b32_e32 v0, 7, v186
	v_and_b32_e32 v0, 0xfe780, v0
	v_lshl_add_u64 v[130:131], v[202:203], 0, v[0:1]
	global_load_dwordx4 v[150:153], v[130:131], off
	v_lshl_add_u64 v[132:133], v[200:201], 0, v[0:1]
	global_load_dwordx4 v[158:161], v[132:133], off
	global_load_dwordx4 v[146:149], v[130:131], off offset:2048
	global_load_dwordx4 v[154:157], v[132:133], off offset:2048
	v_or_b32_e32 v130, 0x1000, v0
	v_mov_b32_e32 v131, v1
	v_lshl_add_u64 v[132:133], v[202:203], 0, v[130:131]
	v_lshl_add_u64 v[130:131], v[200:201], 0, v[130:131]
	global_load_dwordx4 v[138:141], v[132:133], off
	global_load_dwordx4 v[142:145], v[130:131], off
	v_or_b32_e32 v0, 0x1800, v0
	v_lshl_add_u64 v[130:131], v[202:203], 0, v[0:1]
	v_lshl_add_u64 v[134:135], v[200:201], 0, v[0:1]
	global_load_dwordx4 v[130:133], v[130:131], off
	s_cmp_lt_i32 s83, 2
	global_load_dwordx4 v[134:137], v[134:135], off
	v_lshl_add_u32 v250, v186, 5, v252
	v_and_b32_e32 v250, 0x3f9e0, v250
	v_lshlrev_b32_e32 v250, 2, v250
	v_mov_b32_e32 v251, 0
	v_lshl_add_u64 v[230:231], v[202:203], 0, v[250:251]
	global_load_dwordx4 v[216:219], v[230:231], off
	global_load_dwordx4 v[234:237], v[230:231], off offset:2048
	v_lshl_add_u64 v[230:231], v[200:201], 0, v[250:251]
	global_load_dwordx4 v[220:223], v[230:231], off
	global_load_dwordx4 v[238:241], v[230:231], off offset:2048
	v_or_b32_e32 v250, 0x1000, v250
	v_lshl_add_u64 v[230:231], v[202:203], 0, v[250:251]
	global_load_dwordx4 v[242:245], v[230:231], off
	v_lshl_add_u64 v[230:231], v[200:201], 0, v[250:251]
	global_load_dwordx4 v[246:249], v[230:231], off
	s_cselect_b64 vcc, -1, 0
	s_and_b32 s6, s83, -2
	s_ashr_i32 s26, s57, 13
	s_add_i32 s26, s26, s6
	v_cndmask_b32_e32 v185, 1.0, v229, vcc
	s_lshl_b32 s36, s26, 3
	s_lshr_b32 s26, s55, 6
	s_waitcnt vmcnt(0)
	v_mul_f32_e32 v206, v185, v206
	s_and_b32 s55, s26, 5
	s_or_b32 s26, s36, s55
	s_ashr_i32 s27, s26, 31
	s_lshl_b64 s[26:27], s[26:27], 20
	v_and_or_b32 v0, v186, s89, v209
	v_mul_f32_e32 v204, v185, v204
	s_add_u32 s26, s50, s26
	s_addc_u32 s27, s51, s27
	v_lshlrev_b32_e32 v0, 7, v0
	s_or_b32 s57, s55, 2
	s_or_b32 s36, s36, s57
	s_ashr_i32 s37, s36, 31
	s_lshl_b64 s[36:37], s[36:37], 20
	s_add_u32 s36, s50, s36
	s_addc_u32 s37, s51, s37
	v_pk_mul_f32 v[212:213], v[124:125], v[160:161]
	v_pk_mul_f32 v[214:215], v[122:123], v[158:159]
	v_pk_fma_f32 v[212:213], v[128:129], v[152:153], v[212:213] neg_lo:[0,0,1] neg_hi:[0,0,1]
	v_pk_fma_f32 v[214:215], v[126:127], v[150:151], v[214:215] neg_lo:[0,0,1] neg_hi:[0,0,1]
	v_pk_mul_f32 v[128:129], v[128:129], v[160:161]
	v_pk_mul_f32 v[126:127], v[126:127], v[158:159]
	v_pk_fma_f32 v[124:125], v[124:125], v[152:153], v[128:129]
	v_pk_fma_f32 v[122:123], v[122:123], v[150:151], v[126:127]
	v_pk_mul_f32 v[124:125], v[206:207], v[124:125] op_sel_hi:[0,1]
	v_pk_mul_f32 v[122:123], v[206:207], v[122:123] op_sel_hi:[0,1]
	v_cvt_pk_bf16_f32 v122, v122, v123
	v_cvt_pk_bf16_f32 v123, v124, v125
	v_pk_mul_f32 v[124:125], v[116:117], v[156:157]
	v_pk_mul_f32 v[128:129], v[114:115], v[154:155]
	v_pk_fma_f32 v[124:125], v[120:121], v[148:149], v[124:125] neg_lo:[0,0,1] neg_hi:[0,0,1]
	v_pk_fma_f32 v[128:129], v[118:119], v[146:147], v[128:129] neg_lo:[0,0,1] neg_hi:[0,0,1]
	v_pk_mul_f32 v[120:121], v[120:121], v[156:157]
	v_pk_mul_f32 v[118:119], v[118:119], v[154:155]
	v_pk_fma_f32 v[116:117], v[116:117], v[148:149], v[120:121]
	v_pk_fma_f32 v[114:115], v[114:115], v[146:147], v[118:119]
	v_pk_mul_f32 v[212:213], v[206:207], v[212:213] op_sel_hi:[0,1]
	v_pk_mul_f32 v[214:215], v[206:207], v[214:215] op_sel_hi:[0,1]
	v_pk_mul_f32 v[124:125], v[204:205], v[124:125] op_sel_hi:[0,1]
	v_pk_mul_f32 v[128:129], v[204:205], v[128:129] op_sel_hi:[0,1]
	v_pk_mul_f32 v[116:117], v[204:205], v[116:117] op_sel_hi:[0,1]
	v_pk_mul_f32 v[114:115], v[204:205], v[114:115] op_sel_hi:[0,1]
	v_cvt_pk_bf16_f32 v126, v214, v215
	v_cvt_pk_bf16_f32 v127, v212, v213
	v_cvt_pk_bf16_f32 v128, v128, v129
	v_cvt_pk_bf16_f32 v129, v124, v125
	v_cvt_pk_bf16_f32 v124, v114, v115
	v_cvt_pk_bf16_f32 v125, v116, v117
	v_lshl_add_u64 v[116:117], s[26:27], 0, v[0:1]
	v_and_b32_e32 v114, 48, v198
	v_mov_b32_e32 v115, v1
	v_lshl_add_u64 v[116:117], v[116:117], 0, v[114:115]
	v_permlane16_swap_b32_e32 v126, v128
	v_permlane16_swap_b32_e32 v127, v129
	v_permlane16_swap_b32_e32 v122, v124
	v_permlane16_swap_b32_e32 v123, v125
	global_store_dwordx4 v[116:117], v[126:129], off
	global_store_dwordx4 v[116:117], v[122:125], off offset:64
	v_pk_mul_f32 v[116:117], v[108:109], v[160:161]
	v_pk_mul_f32 v[118:119], v[106:107], v[158:159]
	v_pk_fma_f32 v[116:117], v[112:113], v[152:153], v[116:117] neg_lo:[0,0,1] neg_hi:[0,0,1]
	v_pk_fma_f32 v[118:119], v[110:111], v[150:151], v[118:119] neg_lo:[0,0,1] neg_hi:[0,0,1]
	v_pk_mul_f32 v[112:113], v[112:113], v[160:161]
	v_pk_mul_f32 v[110:111], v[110:111], v[158:159]
	v_pk_fma_f32 v[108:109], v[108:109], v[152:153], v[112:113]
	v_pk_fma_f32 v[106:107], v[106:107], v[150:151], v[110:111]
	v_pk_mul_f32 v[108:109], v[206:207], v[108:109] op_sel_hi:[0,1]
	v_pk_mul_f32 v[110:111], v[206:207], v[106:107] op_sel_hi:[0,1]
	v_cvt_pk_bf16_f32 v110, v110, v111
	v_cvt_pk_bf16_f32 v111, v108, v109
	v_pk_mul_f32 v[108:109], v[100:101], v[156:157]
	v_pk_mul_f32 v[112:113], v[98:99], v[154:155]
	v_pk_fma_f32 v[108:109], v[104:105], v[148:149], v[108:109] neg_lo:[0,0,1] neg_hi:[0,0,1]
	v_pk_fma_f32 v[112:113], v[102:103], v[146:147], v[112:113] neg_lo:[0,0,1] neg_hi:[0,0,1]
	v_pk_mul_f32 v[104:105], v[104:105], v[156:157]
	v_pk_mul_f32 v[102:103], v[102:103], v[154:155]
	v_pk_mul_f32 v[116:117], v[206:207], v[116:117] op_sel_hi:[0,1]
	v_pk_fma_f32 v[100:101], v[100:101], v[148:149], v[104:105]
	v_pk_fma_f32 v[98:99], v[98:99], v[146:147], v[102:103]
	v_pk_mul_f32 v[118:119], v[206:207], v[118:119] op_sel_hi:[0,1]
	v_cvt_pk_bf16_f32 v107, v116, v117
	v_pk_mul_f32 v[116:117], v[204:205], v[108:109] op_sel_hi:[0,1]
	v_pk_mul_f32 v[108:109], v[204:205], v[112:113] op_sel_hi:[0,1]
	v_pk_mul_f32 v[100:101], v[204:205], v[100:101] op_sel_hi:[0,1]
	v_pk_mul_f32 v[98:99], v[204:205], v[98:99] op_sel_hi:[0,1]
	v_cvt_pk_bf16_f32 v106, v118, v119
	v_cvt_pk_bf16_f32 v108, v108, v109
	v_cvt_pk_bf16_f32 v109, v116, v117
	v_cvt_pk_bf16_f32 v112, v98, v99
	v_cvt_pk_bf16_f32 v113, v100, v101
	v_lshl_add_u64 v[98:99], s[36:37], 0, v[0:1]
	v_pk_mul_f32 v[100:101], v[92:93], v[144:145]
	v_pk_mul_f32 v[102:103], v[90:91], v[142:143]
	v_lshl_add_u64 v[98:99], v[98:99], 0, v[114:115]
	v_permlane16_swap_b32_e32 v106, v108
	v_permlane16_swap_b32_e32 v107, v109
	v_permlane16_swap_b32_e32 v110, v112
	v_permlane16_swap_b32_e32 v111, v113
	v_pk_fma_f32 v[100:101], v[96:97], v[140:141], v[100:101] neg_lo:[0,0,1] neg_hi:[0,0,1]
	v_pk_fma_f32 v[102:103], v[94:95], v[138:139], v[102:103] neg_lo:[0,0,1] neg_hi:[0,0,1]
	v_pk_mul_f32 v[96:97], v[96:97], v[144:145]
	v_pk_mul_f32 v[94:95], v[94:95], v[142:143]
	global_store_dwordx4 v[98:99], v[106:109], off
	global_store_dwordx4 v[98:99], v[110:113], off offset:64
	v_mul_f32_e32 v98, v185, v196
	v_pk_fma_f32 v[92:93], v[92:93], v[140:141], v[96:97]
	v_pk_fma_f32 v[90:91], v[90:91], v[138:139], v[94:95]
	v_pk_mul_f32 v[92:93], v[98:99], v[92:93] op_sel_hi:[0,1]
	v_pk_mul_f32 v[94:95], v[98:99], v[90:91] op_sel_hi:[0,1]
	v_cvt_pk_bf16_f32 v94, v94, v95
	v_cvt_pk_bf16_f32 v95, v92, v93
	v_pk_mul_f32 v[92:93], v[84:85], v[136:137]
	v_pk_mul_f32 v[96:97], v[82:83], v[134:135]
	v_pk_mul_f32 v[100:101], v[98:99], v[100:101] op_sel_hi:[0,1]
	v_pk_fma_f32 v[92:93], v[88:89], v[132:133], v[92:93] neg_lo:[0,0,1] neg_hi:[0,0,1]
	v_pk_fma_f32 v[96:97], v[86:87], v[130:131], v[96:97] neg_lo:[0,0,1] neg_hi:[0,0,1]
	v_pk_mul_f32 v[88:89], v[88:89], v[136:137]
	v_pk_mul_f32 v[86:87], v[86:87], v[134:135]
	v_pk_mul_f32 v[102:103], v[98:99], v[102:103] op_sel_hi:[0,1]
	v_cvt_pk_bf16_f32 v91, v100, v101
	v_mul_f32_e32 v100, v185, v188
	v_pk_fma_f32 v[84:85], v[84:85], v[132:133], v[88:89]
	v_pk_fma_f32 v[82:83], v[82:83], v[130:131], v[86:87]
	v_cvt_pk_bf16_f32 v90, v102, v103
	v_pk_mul_f32 v[102:103], v[100:101], v[92:93] op_sel_hi:[0,1]
	v_pk_mul_f32 v[92:93], v[100:101], v[96:97] op_sel_hi:[0,1]
	v_pk_mul_f32 v[84:85], v[100:101], v[84:85] op_sel_hi:[0,1]
	v_pk_mul_f32 v[82:83], v[100:101], v[82:83] op_sel_hi:[0,1]
	v_or_b32_e32 v0, 0x1000, v0
	v_cvt_pk_bf16_f32 v92, v92, v93
	v_cvt_pk_bf16_f32 v93, v102, v103
	v_cvt_pk_bf16_f32 v96, v82, v83
	v_cvt_pk_bf16_f32 v97, v84, v85
	v_lshl_add_u64 v[82:83], s[26:27], 0, v[0:1]
	v_lshl_add_u64 v[82:83], v[82:83], 0, v[114:115]
	v_permlane16_swap_b32_e32 v90, v92
	v_permlane16_swap_b32_e32 v91, v93
	v_permlane16_swap_b32_e32 v94, v96
	v_permlane16_swap_b32_e32 v95, v97
	global_store_dwordx4 v[82:83], v[90:93], off
	global_store_dwordx4 v[82:83], v[94:97], off offset:64
	v_pk_mul_f32 v[82:83], v[76:77], v[144:145]
	v_pk_mul_f32 v[84:85], v[74:75], v[142:143]
	v_pk_fma_f32 v[82:83], v[80:81], v[140:141], v[82:83] neg_lo:[0,0,1] neg_hi:[0,0,1]
	v_pk_fma_f32 v[84:85], v[78:79], v[138:139], v[84:85] neg_lo:[0,0,1] neg_hi:[0,0,1]
	v_pk_mul_f32 v[80:81], v[80:81], v[144:145]
	v_pk_mul_f32 v[78:79], v[78:79], v[142:143]
	v_pk_fma_f32 v[76:77], v[76:77], v[140:141], v[80:81]
	v_pk_fma_f32 v[74:75], v[74:75], v[138:139], v[78:79]
	v_pk_mul_f32 v[76:77], v[98:99], v[76:77] op_sel_hi:[0,1]
	v_pk_mul_f32 v[78:79], v[98:99], v[74:75] op_sel_hi:[0,1]
	v_cvt_pk_bf16_f32 v78, v78, v79
	v_cvt_pk_bf16_f32 v79, v76, v77
	v_pk_mul_f32 v[76:77], v[68:69], v[136:137]
	v_pk_mul_f32 v[80:81], v[66:67], v[134:135]
	v_pk_fma_f32 v[76:77], v[72:73], v[132:133], v[76:77] neg_lo:[0,0,1] neg_hi:[0,0,1]
	v_pk_fma_f32 v[80:81], v[70:71], v[130:131], v[80:81] neg_lo:[0,0,1] neg_hi:[0,0,1]
	v_pk_mul_f32 v[72:73], v[72:73], v[136:137]
	v_pk_mul_f32 v[70:71], v[70:71], v[134:135]
	v_pk_mul_f32 v[82:83], v[98:99], v[82:83] op_sel_hi:[0,1]
	v_pk_fma_f32 v[68:69], v[68:69], v[132:133], v[72:73]
	v_pk_fma_f32 v[66:67], v[66:67], v[130:131], v[70:71]
	v_pk_mul_f32 v[84:85], v[98:99], v[84:85] op_sel_hi:[0,1]
	v_cvt_pk_bf16_f32 v75, v82, v83
	v_pk_mul_f32 v[82:83], v[100:101], v[76:77] op_sel_hi:[0,1]
	v_pk_mul_f32 v[76:77], v[100:101], v[80:81] op_sel_hi:[0,1]
	v_pk_mul_f32 v[68:69], v[100:101], v[68:69] op_sel_hi:[0,1]
	v_pk_mul_f32 v[66:67], v[100:101], v[66:67] op_sel_hi:[0,1]
	v_cvt_pk_bf16_f32 v74, v84, v85
	v_cvt_pk_bf16_f32 v76, v76, v77
	v_cvt_pk_bf16_f32 v77, v82, v83
	v_cvt_pk_bf16_f32 v80, v66, v67
	v_cvt_pk_bf16_f32 v81, v68, v69
	v_lshl_add_u64 v[66:67], s[36:37], 0, v[0:1]
	v_lshl_add_u32 v0, v186, 5, v252
	v_lshl_add_u64 v[66:67], v[66:67], 0, v[114:115]
	v_permlane16_swap_b32_e32 v74, v76
	v_permlane16_swap_b32_e32 v75, v77
	v_permlane16_swap_b32_e32 v78, v80
	v_permlane16_swap_b32_e32 v79, v81
	v_and_b32_e32 v0, 0x3f9e0, v0
	global_store_dwordx4 v[66:67], v[74:77], off
	global_store_dwordx4 v[66:67], v[78:81], off offset:64
	v_lshlrev_b32_e32 v0, 2, v0
	v_lshl_add_u64 v[66:67], v[202:203], 0, v[0:1]
	v_lshl_add_u64 v[68:69], v[200:201], 0, v[0:1]
	v_or_b32_e32 v66, 0x1000, v0
	v_mov_b32_e32 v67, v1
	v_lshl_add_u64 v[68:69], v[202:203], 0, v[66:67]
	v_lshl_add_u64 v[66:67], v[200:201], 0, v[66:67]
	v_or_b32_e32 v0, 0x1800, v0
	v_lshl_add_u64 v[66:67], v[202:203], 0, v[0:1]
	v_lshl_add_u64 v[74:75], v[200:201], 0, v[0:1]
	global_load_dwordx4 v[66:69], v[66:67], off
	v_ashrrev_i32_e32 v98, 13, v184
	global_load_dwordx4 v[74:77], v[74:75], off
	v_add_lshl_u32 v99, v98, s6, 3
	v_mul_f32_e32 v98, v185, v182
	v_and_or_b32 v0, v184, s89, v209
	v_lshlrev_b32_e32 v0, 7, v0
	s_waitcnt vmcnt(6)
	v_pk_mul_f32 v[100:101], v[60:61], v[222:223]
	v_pk_mul_f32 v[102:103], v[58:59], v[220:221]
	v_pk_fma_f32 v[100:101], v[64:65], v[218:219], v[100:101] neg_lo:[0,0,1] neg_hi:[0,0,1]
	v_pk_fma_f32 v[102:103], v[62:63], v[216:217], v[102:103] neg_lo:[0,0,1] neg_hi:[0,0,1]
	v_pk_mul_f32 v[64:65], v[64:65], v[222:223]
	v_pk_mul_f32 v[62:63], v[62:63], v[220:221]
	v_pk_fma_f32 v[60:61], v[60:61], v[218:219], v[64:65]
	v_pk_fma_f32 v[58:59], v[58:59], v[216:217], v[62:63]
	s_waitcnt vmcnt(4)
	v_pk_mul_f32 v[64:65], v[50:51], v[238:239]
	v_pk_mul_f32 v[100:101], v[98:99], v[100:101] op_sel_hi:[0,1]
	v_pk_mul_f32 v[60:61], v[98:99], v[60:61] op_sel_hi:[0,1]
	v_pk_mul_f32 v[62:63], v[98:99], v[58:59] op_sel_hi:[0,1]
	v_pk_fma_f32 v[64:65], v[54:55], v[234:235], v[64:65] neg_lo:[0,0,1] neg_hi:[0,0,1]
	v_pk_mul_f32 v[54:55], v[54:55], v[238:239]
	v_cvt_pk_bf16_f32 v59, v100, v101
	v_cvt_pk_bf16_f32 v62, v62, v63
	v_cvt_pk_bf16_f32 v63, v60, v61
	v_mul_f32_e32 v100, v185, v180
	v_pk_mul_f32 v[60:61], v[52:53], v[240:241]
	v_pk_fma_f32 v[50:51], v[50:51], v[234:235], v[54:55]
	v_pk_mul_f32 v[102:103], v[98:99], v[102:103] op_sel_hi:[0,1]
	v_pk_fma_f32 v[60:61], v[56:57], v[236:237], v[60:61] neg_lo:[0,0,1] neg_hi:[0,0,1]
	v_pk_mul_f32 v[50:51], v[100:101], v[50:51] op_sel_hi:[0,1]
	v_cvt_pk_bf16_f32 v58, v102, v103
	v_pk_mul_f32 v[102:103], v[100:101], v[60:61] op_sel_hi:[0,1]
	v_pk_mul_f32 v[60:61], v[100:101], v[64:65] op_sel_hi:[0,1]
	v_cvt_pk_bf16_f32 v64, v50, v51
	v_or_b32_e32 v50, s55, v99
	v_pk_mul_f32 v[56:57], v[56:57], v[240:241]
	v_ashrrev_i32_e32 v51, 31, v50
	v_pk_fma_f32 v[52:53], v[52:53], v[236:237], v[56:57]
	v_lshlrev_b64 v[50:51], 20, v[50:51]
	v_pk_mul_f32 v[52:53], v[100:101], v[52:53] op_sel_hi:[0,1]
	v_lshl_add_u64 v[50:51], s[50:51], 0, v[50:51]
	v_cvt_pk_bf16_f32 v60, v60, v61
	v_cvt_pk_bf16_f32 v61, v102, v103
	v_cvt_pk_bf16_f32 v65, v52, v53
	v_lshl_add_u64 v[52:53], v[50:51], 0, v[0:1]
	v_lshl_add_u64 v[52:53], v[52:53], 0, v[114:115]
	v_permlane16_swap_b32_e32 v58, v60
	v_permlane16_swap_b32_e32 v59, v61
	v_permlane16_swap_b32_e32 v62, v64
	v_permlane16_swap_b32_e32 v63, v65
	global_store_dwordx4 v[52:53], v[58:61], off
	global_store_dwordx4 v[52:53], v[62:65], off offset:64
	v_pk_mul_f32 v[52:53], v[44:45], v[222:223]
	v_pk_mul_f32 v[54:55], v[42:43], v[220:221]
	v_pk_fma_f32 v[52:53], v[48:49], v[218:219], v[52:53] neg_lo:[0,0,1] neg_hi:[0,0,1]
	v_pk_fma_f32 v[54:55], v[46:47], v[216:217], v[54:55] neg_lo:[0,0,1] neg_hi:[0,0,1]
	v_pk_mul_f32 v[48:49], v[48:49], v[222:223]
	v_pk_mul_f32 v[46:47], v[46:47], v[220:221]
	v_pk_fma_f32 v[44:45], v[44:45], v[218:219], v[48:49]
	v_pk_fma_f32 v[42:43], v[42:43], v[216:217], v[46:47]
	v_pk_mul_f32 v[48:49], v[34:35], v[238:239]
	v_pk_mul_f32 v[44:45], v[98:99], v[44:45] op_sel_hi:[0,1]
	v_pk_mul_f32 v[46:47], v[98:99], v[42:43] op_sel_hi:[0,1]
	v_pk_fma_f32 v[48:49], v[38:39], v[234:235], v[48:49] neg_lo:[0,0,1] neg_hi:[0,0,1]
	v_pk_mul_f32 v[38:39], v[38:39], v[238:239]
	v_cvt_pk_bf16_f32 v46, v46, v47
	v_cvt_pk_bf16_f32 v47, v44, v45
	v_pk_mul_f32 v[44:45], v[36:37], v[240:241]
	v_pk_fma_f32 v[34:35], v[34:35], v[234:235], v[38:39]
	v_pk_mul_f32 v[52:53], v[98:99], v[52:53] op_sel_hi:[0,1]
	v_pk_fma_f32 v[44:45], v[40:41], v[236:237], v[44:45] neg_lo:[0,0,1] neg_hi:[0,0,1]
	v_pk_mul_f32 v[34:35], v[100:101], v[34:35] op_sel_hi:[0,1]
	v_cvt_pk_bf16_f32 v43, v52, v53
	v_pk_mul_f32 v[52:53], v[100:101], v[44:45] op_sel_hi:[0,1]
	v_pk_mul_f32 v[44:45], v[100:101], v[48:49] op_sel_hi:[0,1]
	v_cvt_pk_bf16_f32 v48, v34, v35
	v_or_b32_e32 v34, s57, v99
	v_pk_mul_f32 v[40:41], v[40:41], v[240:241]
	v_ashrrev_i32_e32 v35, 31, v34
	v_pk_fma_f32 v[36:37], v[36:37], v[236:237], v[40:41]
	v_lshlrev_b64 v[34:35], 20, v[34:35]
	v_pk_mul_f32 v[54:55], v[98:99], v[54:55] op_sel_hi:[0,1]
	v_pk_mul_f32 v[36:37], v[100:101], v[36:37] op_sel_hi:[0,1]
	v_lshl_add_u64 v[34:35], s[50:51], 0, v[34:35]
	v_cvt_pk_bf16_f32 v42, v54, v55
	v_cvt_pk_bf16_f32 v44, v44, v45
	v_cvt_pk_bf16_f32 v45, v52, v53
	v_cvt_pk_bf16_f32 v49, v36, v37
	v_lshl_add_u64 v[36:37], v[34:35], 0, v[0:1]
	s_waitcnt vmcnt(4)
	v_pk_mul_f32 v[38:39], v[28:29], v[248:249]
	v_pk_mul_f32 v[40:41], v[26:27], v[246:247]
	v_lshl_add_u64 v[36:37], v[36:37], 0, v[114:115]
	v_permlane16_swap_b32_e32 v42, v44
	v_permlane16_swap_b32_e32 v43, v45
	v_permlane16_swap_b32_e32 v46, v48
	v_permlane16_swap_b32_e32 v47, v49
	v_pk_fma_f32 v[38:39], v[32:33], v[244:245], v[38:39] neg_lo:[0,0,1] neg_hi:[0,0,1]
	v_pk_fma_f32 v[40:41], v[30:31], v[242:243], v[40:41] neg_lo:[0,0,1] neg_hi:[0,0,1]
	v_pk_mul_f32 v[32:33], v[32:33], v[248:249]
	v_pk_mul_f32 v[30:31], v[30:31], v[246:247]
	global_store_dwordx4 v[36:37], v[42:45], off
	global_store_dwordx4 v[36:37], v[46:49], off offset:64
	v_mul_f32_e32 v36, v185, v178
	v_pk_fma_f32 v[28:29], v[28:29], v[244:245], v[32:33]
	v_pk_fma_f32 v[26:27], v[26:27], v[242:243], v[30:31]
	v_pk_mul_f32 v[28:29], v[36:37], v[28:29] op_sel_hi:[0,1]
	v_pk_mul_f32 v[30:31], v[36:37], v[26:27] op_sel_hi:[0,1]
	v_cvt_pk_bf16_f32 v30, v30, v31
	v_cvt_pk_bf16_f32 v31, v28, v29
	s_waitcnt vmcnt(4)
	v_pk_mul_f32 v[28:29], v[20:21], v[76:77]
	v_pk_mul_f32 v[32:33], v[18:19], v[74:75]
	v_pk_mul_f32 v[38:39], v[36:37], v[38:39] op_sel_hi:[0,1]
	v_pk_fma_f32 v[28:29], v[24:25], v[68:69], v[28:29] neg_lo:[0,0,1] neg_hi:[0,0,1]
	v_pk_fma_f32 v[32:33], v[22:23], v[66:67], v[32:33] neg_lo:[0,0,1] neg_hi:[0,0,1]
	v_pk_mul_f32 v[24:25], v[24:25], v[76:77]
	v_pk_mul_f32 v[22:23], v[22:23], v[74:75]
	v_pk_mul_f32 v[40:41], v[36:37], v[40:41] op_sel_hi:[0,1]
	v_cvt_pk_bf16_f32 v27, v38, v39
	v_mul_f32_e32 v38, v185, v176
	v_pk_fma_f32 v[20:21], v[20:21], v[68:69], v[24:25]
	v_pk_fma_f32 v[18:19], v[18:19], v[66:67], v[22:23]
	v_cvt_pk_bf16_f32 v26, v40, v41
	v_pk_mul_f32 v[40:41], v[38:39], v[28:29] op_sel_hi:[0,1]
	v_pk_mul_f32 v[28:29], v[38:39], v[32:33] op_sel_hi:[0,1]
	v_pk_mul_f32 v[20:21], v[38:39], v[20:21] op_sel_hi:[0,1]
	v_pk_mul_f32 v[18:19], v[38:39], v[18:19] op_sel_hi:[0,1]
	v_or_b32_e32 v0, 0x1000, v0
	v_cvt_pk_bf16_f32 v28, v28, v29
	v_cvt_pk_bf16_f32 v29, v40, v41
	v_cvt_pk_bf16_f32 v32, v18, v19
	v_cvt_pk_bf16_f32 v33, v20, v21
	v_lshl_add_u64 v[18:19], v[50:51], 0, v[0:1]
	v_lshl_add_u64 v[18:19], v[18:19], 0, v[114:115]
	v_permlane16_swap_b32_e32 v26, v28
	v_permlane16_swap_b32_e32 v27, v29
	v_permlane16_swap_b32_e32 v30, v32
	v_permlane16_swap_b32_e32 v31, v33
	global_store_dwordx4 v[18:19], v[26:29], off
	global_store_dwordx4 v[18:19], v[30:33], off offset:64
	v_pk_mul_f32 v[18:19], v[12:13], v[248:249]
	v_pk_mul_f32 v[20:21], v[10:11], v[246:247]
	v_pk_fma_f32 v[18:19], v[16:17], v[244:245], v[18:19] neg_lo:[0,0,1] neg_hi:[0,0,1]
	v_pk_fma_f32 v[20:21], v[14:15], v[242:243], v[20:21] neg_lo:[0,0,1] neg_hi:[0,0,1]
	v_pk_mul_f32 v[16:17], v[16:17], v[248:249]
	v_pk_mul_f32 v[14:15], v[14:15], v[246:247]
	v_pk_fma_f32 v[12:13], v[12:13], v[244:245], v[16:17]
	v_pk_fma_f32 v[10:11], v[10:11], v[242:243], v[14:15]
	v_pk_mul_f32 v[12:13], v[36:37], v[12:13] op_sel_hi:[0,1]
	v_pk_mul_f32 v[14:15], v[36:37], v[10:11] op_sel_hi:[0,1]
	v_cvt_pk_bf16_f32 v14, v14, v15
	v_cvt_pk_bf16_f32 v15, v12, v13
	v_pk_mul_f32 v[12:13], v[4:5], v[76:77]
	v_pk_mul_f32 v[16:17], v[2:3], v[74:75]
	v_pk_fma_f32 v[12:13], v[8:9], v[68:69], v[12:13] neg_lo:[0,0,1] neg_hi:[0,0,1]
	v_pk_fma_f32 v[16:17], v[6:7], v[66:67], v[16:17] neg_lo:[0,0,1] neg_hi:[0,0,1]
	v_pk_mul_f32 v[8:9], v[8:9], v[76:77]
	v_pk_mul_f32 v[6:7], v[6:7], v[74:75]
	v_pk_mul_f32 v[18:19], v[36:37], v[18:19] op_sel_hi:[0,1]
	v_pk_fma_f32 v[4:5], v[4:5], v[68:69], v[8:9]
	v_pk_fma_f32 v[2:3], v[2:3], v[66:67], v[6:7]
	v_pk_mul_f32 v[20:21], v[36:37], v[20:21] op_sel_hi:[0,1]
	v_cvt_pk_bf16_f32 v11, v18, v19
	v_pk_mul_f32 v[18:19], v[38:39], v[12:13] op_sel_hi:[0,1]
	v_pk_mul_f32 v[12:13], v[38:39], v[16:17] op_sel_hi:[0,1]
	v_pk_mul_f32 v[4:5], v[38:39], v[4:5] op_sel_hi:[0,1]
	v_pk_mul_f32 v[2:3], v[38:39], v[2:3] op_sel_hi:[0,1]
	v_cvt_pk_bf16_f32 v10, v20, v21
	v_cvt_pk_bf16_f32 v12, v12, v13
	v_cvt_pk_bf16_f32 v13, v18, v19
	v_cvt_pk_bf16_f32 v16, v2, v3
	v_cvt_pk_bf16_f32 v17, v4, v5
	v_lshl_add_u64 v[2:3], v[34:35], 0, v[0:1]
	v_lshl_add_u64 v[2:3], v[2:3], 0, v[114:115]
	v_permlane16_swap_b32_e32 v10, v12
	v_permlane16_swap_b32_e32 v11, v13
	v_permlane16_swap_b32_e32 v14, v16
	v_permlane16_swap_b32_e32 v15, v17
	global_store_dwordx4 v[2:3], v[10:13], off
	global_store_dwordx4 v[2:3], v[14:17], off offset:64
	s_andn2_b64 vcc, exec, s[38:39]
	s_mov_b64 s[26:27], -1
	s_cbranch_vccnz .LBB0_665
